# unit deal: the 12 layer-0 ctx NA units go to workgroups vb 20..31 (no 4th q up-projection unit there) instead of vb 0..11
# speedup vs baseline: 1.0121x; 1.0121x over previous
; #define REP(x) for (int rep_ = 0; rep_ < ((DBL_PH) == (x) ? 2 : 1); ++rep_)
; __global__ void __launch_bounds__(NTHREADS, 2) fwd(const Params p) {
;     ...
;             { const int nun = 768 + (layer == 0 ? 12 : 0);
;               REP(32) for (int u = bid; u < nun; u += nb) { if (u < 768) { const int bh = u >> 6, rg = u & 63; na_unit(lp, layer, bh / 6, bh % 6, rg, false, lds); } else { const int bh = u - 768; na_unit(lp, layer, bh / 6, bh % 6, 0, true, lds); } } }
.LBB0_653:
	v_readlane_b32 s2, v253, 43
	s_add_i32 s13, s13, s94
	s_add_i32 s12, s12, s2
	s_cmpk_lt_i32 s13, 0x300
	s_cbranch_scc1 .Lna_deal_reg
	s_add_i32 s13, s13, -20
	s_add_i32 s12, s12, 0xffffffb0
	s_cmpk_lt_i32 s13, 0x300
	s_cbranch_scc0 .Lna_deal_reg
	s_mov_b32 s13, s29
.Lna_deal_reg:
	s_cmp_ge_i32 s13, s29
	s_waitcnt lgkmcnt(0)
	s_cbranch_scc1 .LBB0_688
